# window/SWA: group weight loads issued after the unit prologue wait, first three tile waits counted past them; expert-1 SwiGLU min reads accumulators directly
# speedup vs baseline: 1.0078x; 1.0078x over previous
.LBB0_507:
	s_ashr_i32 s19, s19, 3
	s_andn2_b32 s19, s19, 31
	v_and_b32_e32 v99, 31, v4
	s_add_i32 s20, s19, s20
	v_or_b32_e32 v6, s20, v99
	v_ashrrev_i32_e32 v7, 31, v6
	s_and_b32 s18, s18, 3
	s_lshl_b32 s21, s21, 2
	v_lshl_add_u64 v[92:93], v[6:7], 0, s[82:83]
	v_mov_b64_e32 v[6:7], s[8:9]
	s_or_b32 s18, s18, s21
	v_mad_u64_u32 v[6:7], s[22:23], v92, s70, v[6:7]
	v_bfe_u32 v98, v4, 5, 1
	v_mad_i32_i24 v7, v93, s70, v7
	s_lshl_b32 s82, s18, 7
	v_lshl_add_u64 v[6:7], v[6:7], 0, s[82:83]
	v_lshlrev_b32_e32 v2, 4, v98
	v_lshl_add_u64 v[6:7], v[6:7], 0, v[2:3]
	s_mov_b64 s[22:23], 0x1200
	s_movk_i32 s21, 0x1000
	v_lshl_add_u64 v[124:125], v[6:7], 0, s[22:23]
	v_add_co_u32_e32 v6, vcc, s21, v6
	s_cmp_lt_i32 s17, 0
	s_nop 0
	v_addc_co_u32_e32 v7, vcc, 0, v7, vcc
	global_load_dwordx4 v[66:69], v[124:125], off offset:32
	global_load_dwordx4 v[70:73], v[124:125], off offset:64
	global_load_dwordx4 v[74:77], v[6:7], off offset:512
	global_load_dwordx4 v[78:81], v[124:125], off offset:96
	s_waitcnt vmcnt(0)
	v_mov_b32_e32 v90, v122
	v_min_u32_e32 v91, 0xc00, v123
	s_mov_b32 s32, 0
	s_cmpk_gt_i32 s16, 0xbff
	s_cbranch_scc1 .Lpf_win_skip
	s_mul_hi_i32 s84, s16, 0x2aaaaaab
	s_lshr_b32 s84, s84, 4
	s_mul_i32 s85, s84, 0xffffffa0
	s_add_i32 s85, s85, s16
	v_readlane_b32 s87, v254, 7
	v_readlane_b32 s88, v253, 1
	v_readlane_b32 s89, v253, 2
	s_lshl_b32 s86, s16, 7
	s_and_b32 s86, s86, 0x380
	v_ashrrev_i32_e32 v238, 2, v0
	v_and_b32_e32 v238, -4, v238
	v_add_u32_e32 v238, s86, v238
	v_lshlrev_b32_e32 v240, 4, v0
	v_and_b32_e32 v240, 0xf0, v240
	s_lshl_b32 s87, s87, 5
	s_add_i32 s92, s84, s87
	s_mov_b32 s93, 0
	s_mov_b32 s32, 3
	s_cmp_gt_i32 s85, 63
	s_cbranch_scc1 .Lpf_win_w2
	s_load_dwordx2 s[90:91], s[88:89], 0xa0
	s_lshl_b64 s[92:93], s[92:93], 23
	v_lshlrev_b32_e32 v238, 13, v238
	s_lshl_b32 s86, s85, 4
	s_and_b32 s86, s86, 0xffffff80
	s_lshl_b32 s86, s86, 2
	v_add3_u32 v238, v238, v240, s86
	v_mov_b32_e32 v239, 0
	s_waitcnt lgkmcnt(0)
	s_add_u32 s90, s90, s92
	s_addc_u32 s91, s91, s93
	v_lshl_add_u64 v[238:239], s[90:91], 0, v[238:239]
	s_mov_b64 s[94:95], 0x2000
	v_lshl_add_u64 v[240:241], v[238:239], 0, s[94:95]
	global_load_dwordx4 v[126:129], v[240:241], off nt
	s_mov_b64 s[94:95], 0x4000
	v_lshl_add_u64 v[242:243], v[238:239], 0, s[94:95]
	global_load_dwordx4 v[130:133], v[242:243], off nt
	global_load_dwordx4 v[134:137], v[238:239], off nt
	global_load_dwordx4 v[138:141], v[238:239], off offset:256 nt
	s_mov_b64 s[94:95], 0x6000
	v_lshl_add_u64 v[240:241], v[238:239], 0, s[94:95]
	global_load_dwordx4 v[142:145], v[240:241], off nt
	s_mov_b64 s[94:95], 0x2000
	v_lshl_add_u64 v[242:243], v[238:239], 0, s[94:95]
	global_load_dwordx4 v[146:149], v[242:243], off offset:256 nt
	s_mov_b64 s[94:95], 0x4000
	v_lshl_add_u64 v[240:241], v[238:239], 0, s[94:95]
	global_load_dwordx4 v[168:171], v[240:241], off offset:256 nt
	s_mov_b64 s[94:95], 0x6000
	v_lshl_add_u64 v[242:243], v[238:239], 0, s[94:95]
	global_load_dwordx4 v[172:175], v[242:243], off offset:256 nt
	s_mov_b64 s[94:95], 0x1000
	v_lshl_add_u64 v[240:241], v[238:239], 0, s[94:95]
	global_load_dwordx4 v[176:179], v[240:241], off nt
	s_mov_b64 s[94:95], 0x3000
	v_lshl_add_u64 v[242:243], v[238:239], 0, s[94:95]
	global_load_dwordx4 v[206:209], v[242:243], off nt
	s_mov_b64 s[94:95], 0x5000
	v_lshl_add_u64 v[240:241], v[238:239], 0, s[94:95]
	global_load_dwordx4 v[210:213], v[240:241], off nt
	s_mov_b64 s[94:95], 0x7000
	v_lshl_add_u64 v[242:243], v[238:239], 0, s[94:95]
	global_load_dwordx4 v[214:217], v[242:243], off nt
	s_mov_b64 s[94:95], 0x1000
	v_lshl_add_u64 v[240:241], v[238:239], 0, s[94:95]
	global_load_dwordx4 v[222:225], v[240:241], off offset:256 nt
	s_mov_b64 s[94:95], 0x3000
	v_lshl_add_u64 v[242:243], v[238:239], 0, s[94:95]
	global_load_dwordx4 v[226:229], v[242:243], off offset:256 nt
	s_mov_b64 s[94:95], 0x5000
	v_lshl_add_u64 v[240:241], v[238:239], 0, s[94:95]
	global_load_dwordx4 v[230:233], v[240:241], off offset:256 nt
	s_mov_b64 s[94:95], 0x7000
	v_lshl_add_u64 v[242:243], v[238:239], 0, s[94:95]
	global_load_dwordx4 v[234:237], v[242:243], off offset:256 nt
	s_branch .Lpf_win_skip

.Lpf_win_skip:
	s_cmp_lt_i32 s17, 0
	.p2align 8
	s_cbranch_scc1 .LBB0_532
	s_add_i32 s22, s18, 1
	v_and_b32_e32 v2, 63, v4
	v_cvt_f32_ubyte0_e32 v4, s22
	s_mov_b32 s22, 0x42fc0000
	v_cmp_lt_f32_e32 vcc, s22, v4
	v_mov_b32_e32 v5, 0x42800000
	s_and_b64 s[24:25], vcc, exec
	v_cndmask_b32_e32 v5, 0, v5, vcc
	v_sub_f32_e32 v4, v5, v4
	v_exp_f32_e32 v4, v4
	s_cselect_b32 s23, 0xffffffc0, 0
	v_bfe_u32 v6, v2, 1, 4
	v_cmp_gt_u32_e64 s[36:37], 32, v2
	v_ldexp_f32 v4, v4, s23
	v_mul_f32_e32 v5, 0x43800000, v4
	v_and_b32_e32 v4, 0x7fff0000, v4
	v_or_b32_sdwa v4, v5, v4 dst_sel:DWORD dst_unused:UNUSED_PAD src0_sel:WORD_1 src1_sel:DWORD
	v_lshlrev_b32_e32 v5, 7, v2
	v_and_b32_e32 v100, 0xf00, v5
	v_lshlrev_b32_e32 v5, 3, v2
	v_and_b32_e32 v94, 8, v5
	v_or_b32_e32 v5, v94, v98
	v_bitop3_b32 v7, v94, v6, v98 bitop3:0x36
	v_lshlrev_b32_e32 v101, 4, v7
	v_bitop3_b32 v7, v5, v6, 2 bitop3:0x36
	v_lshlrev_b32_e32 v102, 4, v7
	v_bitop3_b32 v7, v5, v6, 4 bitop3:0x36
	v_bitop3_b32 v5, v5, v6, 6 bitop3:0x36
	v_lshlrev_b32_e32 v104, 4, v5
	v_lshrrev_b32_e32 v5, 2, v2
	v_lshlrev_b32_e32 v103, 4, v7
	v_and_b32_e32 v5, 2, v5
	v_lshrrev_b32_e32 v6, 3, v2
	v_bfe_u32 v7, v2, 1, 1
	v_cndmask_b32_e64 v82, 0, v4, s[36:37]
	v_lshrrev_b32_e32 v4, 1, v2
	v_and_or_b32 v5, v6, 4, v5
	v_and_or_b32 v6, v6, 2, v7
	v_bfe_u32 v2, v2, 3, 1
	v_and_or_b32 v2, v4, 2, v2
	v_lshlrev_b32_e32 v4, 4, v6
	v_lshl_or_b32 v2, v2, 6, v4
	v_lshlrev_b32_e32 v4, 2, v98
	v_lshlrev_b32_e32 v5, 7, v5
	v_or_b32_e32 v105, v2, v5
	v_bitop3_b32 v106, v2, 64, v5 bitop3:0x36
	v_sub_u32_e32 v2, v4, v99
	v_mov_b32_e32 v16, v3
	v_mov_b32_e32 v17, v3
	s_add_i32 s26, s2, s3
	s_sub_i32 s27, 0, s2
	s_lshl_b32 s2, s2, 6
	v_sub_u32_e32 v108, v99, v4
	v_subrev_u32_e32 v109, s19, v2
	v_mov_b32_e32 v2, v3
	v_mov_b32_e32 v4, v3
	v_mov_b32_e32 v5, v3
	v_mov_b32_e32 v6, v3
	v_mov_b32_e32 v7, v3
	v_mov_b32_e32 v8, v3
	v_mov_b32_e32 v9, v3
	v_mov_b32_e32 v10, v3
	v_mov_b32_e32 v11, v3
	v_mov_b32_e32 v12, v3
	v_mov_b32_e32 v13, v3
	v_mov_b32_e32 v14, v3
	v_mov_b32_e32 v15, v3
	v_mov_b64_e32 v[32:33], v[16:17]
	v_mov_b64_e32 v[48:49], v[16:17]
	s_mov_b32 s21, 32
	s_mov_b32 s22, 0
	v_mov_b32_e32 v83, v3
	v_mov_b32_e32 v84, v3
	v_mov_b32_e32 v85, v3
	s_or_b32 s23, s20, 31
	s_add_i32 s24, s20, 0xfffffe01
	s_mov_b32 s25, 3
	s_sub_i32 s26, 0, s26
	s_sub_i32 s28, s27, s3
	s_sub_i32 s29, 0, s2
	v_mov_b32_e32 v110, 0xf149f2ca
	v_mov_b32_e32 v107, 0
	s_mov_b32 s30, 0
	v_mov_b64_e32 v[30:31], v[14:15]
	v_mov_b64_e32 v[28:29], v[12:13]
	v_mov_b64_e32 v[26:27], v[10:11]
	v_mov_b64_e32 v[24:25], v[8:9]
	v_mov_b64_e32 v[22:23], v[6:7]
	v_mov_b64_e32 v[20:21], v[4:5]
	v_mov_b64_e32 v[18:19], v[2:3]
	v_mov_b64_e32 v[46:47], v[14:15]
	v_mov_b64_e32 v[44:45], v[12:13]
	v_mov_b64_e32 v[42:43], v[10:11]
	v_mov_b64_e32 v[40:41], v[8:9]
	v_mov_b64_e32 v[38:39], v[6:7]
	v_mov_b64_e32 v[36:37], v[4:5]
	v_mov_b64_e32 v[34:35], v[2:3]
	s_branch .LBB0_511

.LBB0_511:
	s_add_i32 s2, s28, s21
	s_add_i32 s2, s2, -1
	s_cmp_lt_i32 s2, 2
	s_mov_b64 s[2:3], -1
	s_cbranch_scc0 .LBB0_517
	s_add_i32 s2, s26, s21
	s_cmp_lg_u32 s2, 2
	s_mov_b64 s[2:3], -1
	s_cbranch_scc0 .LBB0_514
	s_cmp_gt_u32 s32, 0
	s_cbranch_scc1 .Lw_win_0_hi
	s_waitcnt vmcnt(0)
	s_branch .Lw_win_0_done
.Lw_win_0_hi:
	s_waitcnt vmcnt(16)

.LBB0_514:
	s_andn2_b64 vcc, exec, s[2:3]
	s_cbranch_vccnz .LBB0_516
	s_cmp_gt_u32 s32, 0
	s_cbranch_scc1 .Lw_win_2_hi
	s_waitcnt vmcnt(2)
	s_branch .Lw_win_2_done
.Lw_win_2_hi:
	s_waitcnt vmcnt(18)
.Lw_win_2_done:
.LBB0_516:
	s_mov_b64 s[2:3], 0
.LBB0_517:
	s_andn2_b64 vcc, exec, s[2:3]
	s_cbranch_vccnz .LBB0_519
	s_cmp_gt_u32 s32, 0
	s_cbranch_scc1 .Lw_win_4_hi
	s_waitcnt vmcnt(4)
	s_branch .Lw_win_4_done
.Lw_win_4_hi:
	s_waitcnt vmcnt(20)
.Lw_win_4_done:
.LBB0_519:
	s_cmp_eq_u32 s32, 0
	s_cselect_b32 s84, 0, 1
	s_sub_u32 s32, s32, s84
	s_barrier
	s_add_i32 s2, s29, s22
	s_cmp_gt_i32 s25, s17
	s_cbranch_scc1 .LBB0_521
	s_add_i32 s3, s2, 0x700
	s_mul_hi_i32 s31, s3, 0x3600
	s_mulk_i32 s3, 0x3600
	s_add_u32 s34, s12, s3
	s_addc_u32 s35, s13, s31
	s_add_u32 s38, s14, s3
	s_addc_u32 s39, s15, s31
	s_add_i32 s3, s30, 0xc000
	s_and_b32 s3, s3, 0xc000
	v_add_u32_e32 v4, s3, v97
	v_mov_b32_e32 v2, v95
	v_readfirstlane_b32 s3, v4
	v_add_u32_e32 v4, 0x2000, v4
	s_mov_b32 m0, s3
	v_readfirstlane_b32 s3, v4
	global_load_lds_dwordx4 v2, s[34:35]
	v_mov_b32_e32 v2, v96
	s_mov_b32 m0, s3
	s_nop 0
	global_load_lds_dwordx4 v2, s[38:39]

.LBB0_539:
	v_lshlrev_b32_e32 v36, 4, v38
	v_and_b32_e32 v2, 0xf0, v36
	v_lshl_add_u64 v[28:29], v[4:5], 0, v[2:3]
	v_lshl_add_u64 v[4:5], v[28:29], 0, s[42:43]
	v_lshl_add_u64 v[6:7], v[28:29], 0, s[40:41]
	s_waitcnt vmcnt(4)
	v_mov_b32_e32 v40, v126
	v_mov_b32_e32 v41, v127
	v_mov_b32_e32 v42, v128
	v_mov_b32_e32 v43, v129
	v_mov_b32_e32 v44, v130
	v_mov_b32_e32 v45, v131
	v_mov_b32_e32 v46, v132
	v_mov_b32_e32 v47, v133
	v_lshl_add_u64 v[4:5], v[28:29], 0, s[38:39]
	v_mov_b32_e32 v84, v134
	v_mov_b32_e32 v85, v135
	v_mov_b32_e32 v86, v136
	v_mov_b32_e32 v87, v137
	v_mov_b32_e32 v66, v138
	v_mov_b32_e32 v67, v139
	v_mov_b32_e32 v68, v140
	v_mov_b32_e32 v69, v141
	v_lshl_add_u64 v[6:7], v[28:29], 0, s[36:37]
	v_mov_b32_e32 v76, v142
	v_mov_b32_e32 v77, v143
	v_mov_b32_e32 v78, v144
	v_mov_b32_e32 v79, v145
	v_mov_b32_e32 v70, v146
	v_mov_b32_e32 v71, v147
	v_mov_b32_e32 v72, v148
	v_mov_b32_e32 v73, v149
	v_lshl_add_u64 v[4:5], v[28:29], 0, s[34:35]
	v_lshl_add_u64 v[6:7], v[28:29], 0, s[30:31]
	v_mov_b32_e32 v60, v168
	v_mov_b32_e32 v61, v169
	v_mov_b32_e32 v62, v170
	v_mov_b32_e32 v63, v171
	v_mov_b32_e32 v92, v172
	v_mov_b32_e32 v93, v173
	v_mov_b32_e32 v94, v174
	v_mov_b32_e32 v95, v175
	v_lshl_add_u64 v[4:5], v[28:29], 0, s[28:29]
	v_lshl_add_u64 v[8:9], v[28:29], 0, s[26:27]
	v_lshl_add_u64 v[12:13], v[28:29], 0, s[24:25]
	v_lshl_add_u64 v[16:17], v[28:29], 0, s[22:23]
	v_lshl_add_u64 v[20:21], v[28:29], 0, s[20:21]
	v_lshl_add_u64 v[24:25], v[28:29], 0, s[18:19]
	v_lshl_add_u64 v[30:31], v[28:29], 0, s[16:17]
	v_lshl_add_u64 v[32:33], v[28:29], 0, s[14:15]
	v_mov_b32_e32 v4, v176
	v_mov_b32_e32 v5, v177
	v_mov_b32_e32 v6, v178
	v_mov_b32_e32 v7, v179
	v_mov_b32_e32 v8, v206
	v_mov_b32_e32 v9, v207
	v_mov_b32_e32 v10, v208
	v_mov_b32_e32 v11, v209
	v_mov_b32_e32 v12, v210
	v_mov_b32_e32 v13, v211
	v_mov_b32_e32 v14, v212
	v_mov_b32_e32 v15, v213
	v_mov_b32_e32 v16, v214
	v_mov_b32_e32 v17, v215
	v_mov_b32_e32 v18, v216
	v_mov_b32_e32 v19, v217
	v_mov_b32_e32 v20, v222
	v_mov_b32_e32 v21, v223
	v_mov_b32_e32 v22, v224
	v_mov_b32_e32 v23, v225
	v_mov_b32_e32 v24, v226
	v_mov_b32_e32 v25, v227
	v_mov_b32_e32 v26, v228
	v_mov_b32_e32 v27, v229
	v_mov_b32_e32 v28, v230
	v_mov_b32_e32 v29, v231
	v_mov_b32_e32 v30, v232
	v_mov_b32_e32 v31, v233
	v_mov_b32_e32 v32, v234
	v_mov_b32_e32 v33, v235
	v_mov_b32_e32 v34, v236
	v_mov_b32_e32 v35, v237
	v_ashrrev_i32_e32 v39, 6, v38
	v_lshlrev_b32_e32 v37, 9, v38
	v_bitop3_b32 v39, v39, v38, 7 bitop3:0x78
	v_lshrrev_b32_e32 v2, 2, v38
	v_and_b32_e32 v37, 0x1e00, v37
	v_lshlrev_b32_e32 v39, 4, v39
	v_add3_u32 v39, 0, v37, v39
	v_and_b32_e32 v48, 12, v2
	v_ashrrev_i32_e32 v37, 3, v38
	v_lshrrev_b32_e32 v49, 5, v38
	v_add_u32_e32 v48, v39, v48
	v_and_b32_e32 v2, 0x70, v36
	v_add_u32_e32 v36, s44, v37
	s_mov_b64 s[14:15], -1
	s_and_b64 vcc, exec, s[2:3]
	v_lshlrev_b32_e32 v37, 7, v37
	v_xor_b32_e32 v82, v49, v38
	v_mul_f32_e32 v49, 0x42000000, v95
	v_mul_f32_e32 v50, 0x42000000, v63
	v_mul_f32_e32 v52, 0x42000000, v73
	v_mul_f32_e32 v54, 0x42000000, v69
	v_mul_f32_e32 v51, 0x42000000, v94
	v_mul_f32_e32 v53, 0x42000000, v62
	v_mul_f32_e32 v57, 0x42000000, v72
	v_mul_f32_e32 v58, 0x42000000, v68
	v_mul_f32_e32 v55, 0x42000000, v93
	v_mul_f32_e32 v56, 0x42000000, v61
	v_mul_f32_e32 v61, 0x42000000, v71
	v_mul_f32_e32 v62, 0x42000000, v67
	v_mul_f32_e32 v59, 0x42000000, v92
	v_mul_f32_e32 v60, 0x42000000, v60
	v_mul_f32_e32 v64, 0x42000000, v70
	v_mul_f32_e32 v65, 0x42000000, v66
	v_mul_f32_e32 v66, 0x42000000, v79
	v_mul_f32_e32 v67, 0x42000000, v47
	v_mul_f32_e32 v69, 0x42000000, v43
	v_mul_f32_e32 v71, 0x42000000, v87
	v_mul_f32_e32 v68, 0x42000000, v78
	v_mul_f32_e32 v70, 0x42000000, v46
	v_mul_f32_e32 v74, 0x42000000, v42
	v_mul_f32_e32 v75, 0x42000000, v86
	v_mul_f32_e32 v72, 0x42000000, v77
	v_mul_f32_e32 v73, 0x42000000, v45
	v_mul_f32_e32 v78, 0x42000000, v41
	v_mul_f32_e32 v79, 0x42000000, v85
	v_mul_f32_e32 v76, 0x42000000, v76
	v_mul_f32_e32 v77, 0x42000000, v44
	v_mul_f32_e32 v80, 0x42000000, v40
	v_mul_f32_e32 v81, 0x42000000, v84
	v_add_u32_e32 v63, 0x2000, v48
	v_add_u32_e32 v47, 0x4000, v48
	v_add_u32_e32 v46, 0x6000, v48
	s_barrier
	s_cbranch_vccz .LBB0_541
	v_mov_b32_e32 v118, v3
	v_mov_b32_e32 v119, v3
	v_cvt_pk_fp8_f32 v118, v81, v80
	v_cvt_pk_fp8_f32 v119, v79, v78
	v_mul_f32_e32 v116, 0x42000000, v8
	v_mul_f32_e32 v117, 0x42000000, v4
	v_cvt_pk_fp8_f32 v118, v77, v76 op_sel:[0,0,1]
	v_cvt_pk_fp8_f32 v119, v73, v72 op_sel:[0,0,1]
	v_mul_f32_e32 v114, 0x42000000, v16
	v_mul_f32_e32 v115, 0x42000000, v12
	v_mul_f32_e32 v112, 0x42000000, v9
	ds_write2_b32 v48, v118, v119 offset1:32
	v_mov_b32_e32 v118, v3
	v_mov_b32_e32 v119, v3
	v_cvt_pk_fp8_f32 v118, v75, v74
	v_cvt_pk_fp8_f32 v119, v71, v69
	v_mul_f32_e32 v113, 0x42000000, v5
	v_mul_f32_e32 v110, 0x42000000, v17
	v_cvt_pk_fp8_f32 v118, v70, v68 op_sel:[0,0,1]
	v_cvt_pk_fp8_f32 v119, v67, v66 op_sel:[0,0,1]
	v_mul_f32_e32 v111, 0x42000000, v13
	v_mul_f32_e32 v108, 0x42000000, v10
	v_mul_f32_e32 v109, 0x42000000, v6
	ds_write2_b32 v48, v118, v119 offset0:64 offset1:96
	v_mov_b32_e32 v118, v3
	v_mov_b32_e32 v119, v3
	v_cvt_pk_fp8_f32 v118, v65, v64
	v_cvt_pk_fp8_f32 v119, v62, v61
	v_mul_f32_e32 v106, 0x42000000, v18
	v_mul_f32_e32 v107, 0x42000000, v14
	v_cvt_pk_fp8_f32 v118, v60, v59 op_sel:[0,0,1]
	v_cvt_pk_fp8_f32 v119, v56, v55 op_sel:[0,0,1]
	v_mul_f32_e32 v104, 0x42000000, v11
	v_mul_f32_e32 v105, 0x42000000, v7
	v_mul_f32_e32 v102, 0x42000000, v19
	ds_write2_b32 v63, v118, v119 offset1:32
	v_mov_b32_e32 v118, v3
	v_mov_b32_e32 v119, v3
	v_cvt_pk_fp8_f32 v118, v58, v57
	v_cvt_pk_fp8_f32 v119, v54, v52
	v_mul_f32_e32 v103, 0x42000000, v15
	v_mul_f32_e32 v100, 0x42000000, v24
	v_cvt_pk_fp8_f32 v118, v53, v51 op_sel:[0,0,1]
	v_cvt_pk_fp8_f32 v119, v50, v49 op_sel:[0,0,1]
	v_mul_f32_e32 v101, 0x42000000, v20
	v_mul_f32_e32 v98, 0x42000000, v32
	v_mul_f32_e32 v99, 0x42000000, v28
	ds_write2_b32 v63, v118, v119 offset0:64 offset1:96
	v_mov_b32_e32 v118, v3
	v_cvt_pk_fp8_f32 v118, v117, v116
	v_mul_f32_e32 v96, 0x42000000, v25
	v_mul_f32_e32 v97, 0x42000000, v21
	v_mul_f32_e32 v94, 0x42000000, v33
	v_cvt_pk_fp8_f32 v118, v115, v114 op_sel:[0,0,1]
	v_mov_b32_e32 v114, v3
	v_cvt_pk_fp8_f32 v114, v113, v112
	v_mul_f32_e32 v95, 0x42000000, v29
	v_mul_f32_e32 v92, 0x42000000, v26
	v_mul_f32_e32 v93, 0x42000000, v22
	v_cvt_pk_fp8_f32 v114, v111, v110 op_sel:[0,0,1]
	v_mov_b32_e32 v110, v3
	v_cvt_pk_fp8_f32 v110, v109, v108
	s_lshl_b64 s[2:3], s[12:13], 20
	s_add_u32 s2, s56, s2
	v_lshlrev_b32_e32 v40, 4, v82
	v_cvt_pk_fp8_f32 v110, v107, v106 op_sel:[0,0,1]
	v_mov_b32_e32 v106, v3
	v_cvt_pk_fp8_f32 v106, v105, v104
	v_mul_f32_e32 v88, 0x42000000, v34
	v_mul_f32_e32 v89, 0x42000000, v30
	s_addc_u32 s3, s57, s3
	v_cvt_pk_fp8_f32 v106, v103, v102 op_sel:[0,0,1]
	v_mov_b32_e32 v102, v3
	v_cvt_pk_fp8_f32 v102, v101, v100
	v_and_b32_e32 v40, 0x70, v40
	v_mul_f32_e32 v86, 0x42000000, v27
	v_mul_f32_e32 v87, 0x42000000, v23
	v_cvt_pk_fp8_f32 v102, v99, v98 op_sel:[0,0,1]
	v_mov_b32_e32 v98, v3
	v_cvt_pk_fp8_f32 v98, v97, v96
	s_add_u32 s2, s2, s33
	v_add_u32_e32 v84, 0xfffff800, v36
	v_add_u32_e32 v38, 0xfffff8c0, v36
	v_cvt_pk_fp8_f32 v98, v95, v94 op_sel:[0,0,1]
	v_mov_b32_e32 v94, v3
	v_cvt_pk_fp8_f32 v94, v93, v92
	v_add3_u32 v83, 0, v37, v40
	v_add_u32_e32 v40, 0xfffff880, v36
	v_add_u32_e32 v42, 0xfffff840, v36
	v_cvt_pk_fp8_f32 v94, v89, v88 op_sel:[0,0,1]
	v_mov_b32_e32 v88, v3
	v_cvt_pk_fp8_f32 v88, v87, v86
	s_addc_u32 s3, s3, 0
	v_ashrrev_i32_e32 v39, 31, v38
	v_ashrrev_i32_e32 v41, 31, v40
	v_ashrrev_i32_e32 v43, 31, v42
	v_ashrrev_i32_e32 v85, 31, v84
	v_lshl_add_u64 v[44:45], s[2:3], 0, v[2:3]
	v_lshlrev_b64 v[38:39], 10, v[38:39]
	v_lshlrev_b64 v[40:41], 10, v[40:41]
	v_lshlrev_b64 v[42:43], 10, v[42:43]
	v_lshlrev_b64 v[84:85], 10, v[84:85]
	v_lshl_add_u64 v[38:39], v[44:45], 0, v[38:39]
	v_lshl_add_u64 v[40:41], v[44:45], 0, v[40:41]
	v_lshl_add_u64 v[42:43], v[44:45], 0, v[42:43]
	v_lshl_add_u64 v[44:45], v[44:45], 0, v[84:85]
	v_mul_f32_e32 v84, 0x42000000, v35
	v_mul_f32_e32 v85, 0x42000000, v31
	v_cvt_pk_fp8_f32 v88, v85, v84 op_sel:[0,0,1]
	ds_write2_b32 v47, v118, v114 offset1:32
	ds_write2_b32 v47, v110, v106 offset0:64 offset1:96
	ds_write2_b32 v46, v102, v98 offset1:32
	ds_write2_b32 v46, v94, v88 offset0:64 offset1:96
	s_waitcnt lgkmcnt(0)
	s_barrier
	ds_read_b128 v[84:87], v83
	s_mov_b64 s[14:15], 0
	s_waitcnt lgkmcnt(0)
	global_store_dwordx4 v[44:45], v[84:87], off
	ds_read_b128 v[84:87], v83 offset:8192
	s_waitcnt lgkmcnt(0)
	global_store_dwordx4 v[42:43], v[84:87], off
	ds_read_b128 v[42:45], v83 offset:16384
	s_waitcnt lgkmcnt(0)
	global_store_dwordx4 v[40:41], v[42:45], off
	ds_read_b128 v[40:43], v83 offset:24576
	s_waitcnt lgkmcnt(0)
	global_store_dwordx4 v[38:39], v[40:43], off
	s_barrier

.LBB0_768:
	s_and_b32 s14, s14, 3
	s_lshl_b32 s17, s17, 2
	s_or_b32 s14, s14, s17
	s_add_i32 s17, s14, 1
	v_cvt_f32_ubyte0_e32 v2, s17
	s_mov_b32 s17, 0x42fc0000
	v_cmp_lt_f32_e32 vcc, s17, v2
	v_mov_b32_e32 v5, 0x42800000
	s_ashr_i32 s15, s15, 3
	v_cndmask_b32_e32 v5, 0, v5, vcc
	s_andn2_b32 s15, s15, 31
	v_sub_f32_e32 v2, v5, v2
	v_and_b32_e32 v102, 31, v4
	s_add_i32 s16, s15, s16
	v_exp_f32_e32 v2, v2
	v_or_b32_e32 v94, s16, v102
	s_and_b64 s[18:19], vcc, exec
	v_ashrrev_i32_e32 v95, 31, v94
	s_cselect_b32 s18, 0xffffffc0, 0
	v_lshl_add_u64 v[92:93], v[94:95], 0, s[82:83]
	v_mov_b64_e32 v[6:7], s[50:51]
	v_ldexp_f32 v100, v2, s18
	v_mad_u64_u32 v[6:7], s[18:19], v92, s70, v[6:7]
	v_bfe_u32 v101, v4, 5, 1
	v_mad_i32_i24 v7, v93, s70, v7
	s_lshl_b32 s82, s14, 7
	v_lshl_add_u64 v[6:7], v[6:7], 0, s[82:83]
	v_lshlrev_b32_e32 v2, 4, v101
	v_lshl_add_u64 v[6:7], v[6:7], 0, v[2:3]
	global_load_dwordx4 v[66:69], v[6:7], off
	global_load_dwordx4 v[70:73], v[6:7], off offset:32
	global_load_dwordx4 v[74:77], v[6:7], off offset:64
	global_load_dwordx4 v[78:81], v[6:7], off offset:96
	s_load_dwordx2 s[18:19], s[48:49], 0x40
	s_or_b32 s82, s14, s33
	s_lshl_b64 s[20:21], s[82:83], 2
	s_mov_b32 s17, 0
	s_waitcnt lgkmcnt(0)
	s_add_u32 s18, s18, s20
	s_addc_u32 s19, s19, s21
	global_load_dword v95, v3, s[18:19]
	s_cmp_lt_i32 s13, 0
	s_waitcnt vmcnt(0)
	v_mov_b32_e32 v90, v122
	v_min_u32_e32 v91, 0xc00, v123
	s_mov_b32 s32, 0
	s_cmpk_gt_i32 s12, 0xbff
	s_cbranch_scc1 .Lpf_swa_skip
	s_mul_hi_i32 s84, s12, 0x2aaaaaab
	s_lshr_b32 s84, s84, 4
	s_mul_i32 s85, s84, 0xffffffa0
	s_add_i32 s85, s85, s12
	v_readlane_b32 s87, v254, 7
	v_readlane_b32 s88, v253, 1
	v_readlane_b32 s89, v253, 2
	s_lshl_b32 s86, s12, 7
	s_and_b32 s86, s86, 0x380
	v_ashrrev_i32_e32 v238, 2, v0
	v_and_b32_e32 v238, -4, v238
	v_add_u32_e32 v238, s86, v238
	v_lshlrev_b32_e32 v240, 4, v0
	v_and_b32_e32 v240, 0xf0, v240
	s_lshl_b32 s87, s87, 5
	s_add_i32 s92, s84, s87
	s_mov_b32 s93, 0
	s_mov_b32 s32, 3
	s_cmp_gt_i32 s85, 63
	s_cbranch_scc1 .Lpf_swa_w2
	s_load_dwordx2 s[90:91], s[88:89], 0xa0
	s_lshl_b64 s[92:93], s[92:93], 23
	v_lshlrev_b32_e32 v238, 13, v238
	s_lshl_b32 s86, s85, 4
	s_and_b32 s86, s86, 0xffffff80
	s_lshl_b32 s86, s86, 2
	v_add3_u32 v238, v238, v240, s86
	v_mov_b32_e32 v239, 0
	s_waitcnt lgkmcnt(0)
	s_add_u32 s90, s90, s92
	s_addc_u32 s91, s91, s93
	v_lshl_add_u64 v[238:239], s[90:91], 0, v[238:239]
	s_mov_b64 s[94:95], 0x2000
	v_lshl_add_u64 v[240:241], v[238:239], 0, s[94:95]
	global_load_dwordx4 v[126:129], v[240:241], off nt
	s_mov_b64 s[94:95], 0x4000
	v_lshl_add_u64 v[242:243], v[238:239], 0, s[94:95]
	global_load_dwordx4 v[130:133], v[242:243], off nt
	global_load_dwordx4 v[134:137], v[238:239], off nt
	global_load_dwordx4 v[138:141], v[238:239], off offset:256 nt
	s_mov_b64 s[94:95], 0x6000
	v_lshl_add_u64 v[240:241], v[238:239], 0, s[94:95]
	global_load_dwordx4 v[142:145], v[240:241], off nt
	s_mov_b64 s[94:95], 0x2000
	v_lshl_add_u64 v[242:243], v[238:239], 0, s[94:95]
	global_load_dwordx4 v[146:149], v[242:243], off offset:256 nt
	s_mov_b64 s[94:95], 0x4000
	v_lshl_add_u64 v[240:241], v[238:239], 0, s[94:95]
	global_load_dwordx4 v[168:171], v[240:241], off offset:256 nt
	s_mov_b64 s[94:95], 0x6000
	v_lshl_add_u64 v[242:243], v[238:239], 0, s[94:95]
	global_load_dwordx4 v[172:175], v[242:243], off offset:256 nt
	s_mov_b64 s[94:95], 0x1000
	v_lshl_add_u64 v[240:241], v[238:239], 0, s[94:95]
	global_load_dwordx4 v[176:179], v[240:241], off nt
	s_mov_b64 s[94:95], 0x3000
	v_lshl_add_u64 v[242:243], v[238:239], 0, s[94:95]
	global_load_dwordx4 v[206:209], v[242:243], off nt
	s_mov_b64 s[94:95], 0x5000
	v_lshl_add_u64 v[240:241], v[238:239], 0, s[94:95]
	global_load_dwordx4 v[210:213], v[240:241], off nt
	s_mov_b64 s[94:95], 0x7000
	v_lshl_add_u64 v[242:243], v[238:239], 0, s[94:95]
	global_load_dwordx4 v[214:217], v[242:243], off nt
	s_mov_b64 s[94:95], 0x1000
	v_lshl_add_u64 v[240:241], v[238:239], 0, s[94:95]
	global_load_dwordx4 v[222:225], v[240:241], off offset:256 nt
	s_mov_b64 s[94:95], 0x3000
	v_lshl_add_u64 v[242:243], v[238:239], 0, s[94:95]
	global_load_dwordx4 v[226:229], v[242:243], off offset:256 nt
	s_mov_b64 s[94:95], 0x5000
	v_lshl_add_u64 v[240:241], v[238:239], 0, s[94:95]
	global_load_dwordx4 v[230:233], v[240:241], off offset:256 nt
	s_mov_b64 s[94:95], 0x7000
	v_lshl_add_u64 v[242:243], v[238:239], 0, s[94:95]
	global_load_dwordx4 v[234:237], v[242:243], off offset:256 nt
	s_branch .Lpf_swa_skip

.Lpf_swa_skip:
	s_cmp_lt_i32 s13, 0
	.p2align 8
	s_cbranch_scc1 .LBB0_793
	v_and_b32_e32 v2, 63, v4
	v_mul_f32_e32 v4, 0x43800000, v100
	v_and_b32_e32 v5, 0x7fff0000, v100
	v_or_b32_sdwa v4, v4, v5 dst_sel:DWORD dst_unused:UNUSED_PAD src0_sel:WORD_1 src1_sel:DWORD
	v_lshlrev_b32_e32 v5, 7, v2
	v_and_b32_e32 v103, 0xf00, v5
	v_lshlrev_b32_e32 v5, 3, v2
	v_and_b32_e32 v96, 8, v5
	v_bfe_u32 v6, v2, 1, 4
	v_or_b32_e32 v5, v96, v101
	v_bitop3_b32 v7, v96, v6, v101 bitop3:0x36
	v_lshlrev_b32_e32 v104, 4, v7
	v_bitop3_b32 v7, v5, v6, 2 bitop3:0x36
	v_lshlrev_b32_e32 v105, 4, v7
	v_bitop3_b32 v7, v5, v6, 4 bitop3:0x36
	v_bitop3_b32 v5, v5, v6, 6 bitop3:0x36
	v_lshlrev_b32_e32 v107, 4, v5
	v_lshrrev_b32_e32 v5, 2, v2
	v_cmp_gt_u32_e64 s[36:37], 32, v2
	v_lshlrev_b32_e32 v106, 4, v7
	v_and_b32_e32 v5, 2, v5
	v_lshrrev_b32_e32 v6, 3, v2
	v_bfe_u32 v7, v2, 1, 1
	v_cndmask_b32_e64 v82, 0, v4, s[36:37]
	v_lshrrev_b32_e32 v4, 1, v2
	v_and_or_b32 v5, v6, 4, v5
	v_and_or_b32 v6, v6, 2, v7
	v_bfe_u32 v2, v2, 3, 1
	v_and_or_b32 v2, v4, 2, v2
	v_lshlrev_b32_e32 v4, 4, v6
	v_lshl_or_b32 v2, v2, 6, v4
	v_lshlrev_b32_e32 v4, 2, v101
	v_lshlrev_b32_e32 v5, 7, v5
	v_or_b32_e32 v109, v2, v5
	v_bitop3_b32 v110, v2, 64, v5 bitop3:0x36
	v_sub_u32_e32 v2, v4, v102
	v_mov_b32_e32 v16, v3
	v_mov_b32_e32 v17, v3
	s_add_i32 s22, s0, s1
	s_sub_i32 s23, 0, s0
	s_lshl_b32 s0, s0, 6
	v_sub_u32_e32 v111, v102, v4
	v_subrev_u32_e32 v112, s15, v2
	v_mov_b32_e32 v2, v3
	v_mov_b32_e32 v4, v3
	v_mov_b32_e32 v5, v3
	v_mov_b32_e32 v6, v3
	v_mov_b32_e32 v7, v3
	v_mov_b32_e32 v8, v3
	v_mov_b32_e32 v9, v3
	v_mov_b32_e32 v10, v3
	v_mov_b32_e32 v11, v3
	v_mov_b32_e32 v12, v3
	v_mov_b32_e32 v13, v3
	v_mov_b32_e32 v14, v3
	v_mov_b32_e32 v15, v3
	v_mov_b64_e32 v[32:33], v[16:17]
	v_mov_b64_e32 v[48:49], v[16:17]
	s_mov_b32 s18, 32
	v_mov_b32_e32 v83, v3
	v_mov_b32_e32 v84, v3
	v_mov_b32_e32 v85, v3
	s_or_b32 s19, s16, 31
	s_add_i32 s20, s16, 0xffffff81
	s_mov_b32 s21, 3
	s_sub_i32 s22, 0, s22
	s_sub_i32 s24, s23, s1
	s_sub_i32 s25, 0, s0
	v_mov_b32_e32 v113, 0xf149f2ca
	v_mov_b32_e32 v108, 0
	s_mov_b32 s26, 0
	v_mov_b64_e32 v[30:31], v[14:15]
	v_mov_b64_e32 v[28:29], v[12:13]
	v_mov_b64_e32 v[26:27], v[10:11]
	v_mov_b64_e32 v[24:25], v[8:9]
	v_mov_b64_e32 v[22:23], v[6:7]
	v_mov_b64_e32 v[20:21], v[4:5]
	v_mov_b64_e32 v[18:19], v[2:3]
	v_mov_b64_e32 v[46:47], v[14:15]
	v_mov_b64_e32 v[44:45], v[12:13]
	v_mov_b64_e32 v[42:43], v[10:11]
	v_mov_b64_e32 v[40:41], v[8:9]
	v_mov_b64_e32 v[38:39], v[6:7]
	v_mov_b64_e32 v[36:37], v[4:5]
	v_mov_b64_e32 v[34:35], v[2:3]
	s_branch .LBB0_772

.LBB0_772:
	s_add_i32 s0, s24, s18
	s_add_i32 s0, s0, -1
	s_cmp_lt_i32 s0, 2
	s_mov_b64 s[0:1], -1
	s_cbranch_scc0 .LBB0_778
	s_add_i32 s0, s22, s18
	s_cmp_lg_u32 s0, 2
	s_mov_b64 s[0:1], -1
	s_cbranch_scc0 .LBB0_775
	s_cmp_gt_u32 s32, 0
	s_cbranch_scc1 .Lw_swa_0_hi
	s_waitcnt vmcnt(0)
	s_branch .Lw_swa_0_done

.LBB0_775:
	s_andn2_b64 vcc, exec, s[0:1]
	s_cbranch_vccnz .LBB0_777
	s_cmp_gt_u32 s32, 0
	s_cbranch_scc1 .Lw_swa_2_hi
	s_waitcnt vmcnt(2)
	s_branch .Lw_swa_2_done

.Lw_swa_2_done:
.LBB0_777:
	s_mov_b64 s[0:1], 0
.LBB0_778:
	s_andn2_b64 vcc, exec, s[0:1]
	s_cbranch_vccnz .LBB0_780
	s_cmp_gt_u32 s32, 0
	s_cbranch_scc1 .Lw_swa_4_hi
	s_waitcnt vmcnt(4)
	s_branch .Lw_swa_4_done

.Lw_swa_4_done:
.LBB0_780:
	s_cmp_eq_u32 s32, 0
	s_cselect_b32 s84, 0, 1
	s_sub_u32 s32, s32, s84
	s_barrier
	s_add_i32 s0, s25, s17
	s_cmp_gt_i32 s21, s13
	s_cbranch_scc1 .LBB0_782
	s_add_i32 s1, s0, 0x700
	s_mul_hi_i32 s27, s1, 0x3600
	s_mulk_i32 s1, 0x3600
	s_add_u32 s28, s2, s1
	s_addc_u32 s29, s3, s27
	s_add_u32 s30, s10, s1
	s_addc_u32 s31, s11, s27
	s_add_i32 s1, s26, 0xc000
	s_and_b32 s1, s1, 0xc000
	v_add_u32_e32 v4, s1, v99
	v_mov_b32_e32 v2, v97
	v_readfirstlane_b32 s1, v4
	v_add_u32_e32 v4, 0x2000, v4
	s_mov_b32 m0, s1
	v_readfirstlane_b32 s1, v4
	global_load_lds_dwordx4 v2, s[28:29]
	v_mov_b32_e32 v2, v98
	s_mov_b32 m0, s1
	s_nop 0
	global_load_lds_dwordx4 v2, s[30:31]

.LBB0_800:
	v_lshlrev_b32_e32 v36, 4, v38
	v_and_b32_e32 v2, 0xf0, v36
	v_lshl_add_u64 v[28:29], v[4:5], 0, v[2:3]
	v_lshl_add_u64 v[4:5], v[28:29], 0, s[38:39]
	v_lshl_add_u64 v[6:7], v[28:29], 0, s[36:37]
	s_waitcnt vmcnt(4)
	v_mov_b32_e32 v40, v126
	v_mov_b32_e32 v41, v127
	v_mov_b32_e32 v42, v128
	v_mov_b32_e32 v43, v129
	v_mov_b32_e32 v44, v130
	v_mov_b32_e32 v45, v131
	v_mov_b32_e32 v46, v132
	v_mov_b32_e32 v47, v133
	v_lshl_add_u64 v[4:5], v[28:29], 0, s[34:35]
	v_mov_b32_e32 v84, v134
	v_mov_b32_e32 v85, v135
	v_mov_b32_e32 v86, v136
	v_mov_b32_e32 v87, v137
	v_mov_b32_e32 v66, v138
	v_mov_b32_e32 v67, v139
	v_mov_b32_e32 v68, v140
	v_mov_b32_e32 v69, v141
	v_lshl_add_u64 v[6:7], v[28:29], 0, s[30:31]
	v_mov_b32_e32 v76, v142
	v_mov_b32_e32 v77, v143
	v_mov_b32_e32 v78, v144
	v_mov_b32_e32 v79, v145
	v_mov_b32_e32 v70, v146
	v_mov_b32_e32 v71, v147
	v_mov_b32_e32 v72, v148
	v_mov_b32_e32 v73, v149
	v_lshl_add_u64 v[4:5], v[28:29], 0, s[28:29]
	v_lshl_add_u64 v[6:7], v[28:29], 0, s[26:27]
	v_mov_b32_e32 v60, v168
	v_mov_b32_e32 v61, v169
	v_mov_b32_e32 v62, v170
	v_mov_b32_e32 v63, v171
	v_mov_b32_e32 v92, v172
	v_mov_b32_e32 v93, v173
	v_mov_b32_e32 v94, v174
	v_mov_b32_e32 v95, v175
	v_lshl_add_u64 v[4:5], v[28:29], 0, s[24:25]
	v_lshl_add_u64 v[8:9], v[28:29], 0, s[22:23]
	v_lshl_add_u64 v[12:13], v[28:29], 0, s[20:21]
	v_lshl_add_u64 v[16:17], v[28:29], 0, s[18:19]
	v_lshl_add_u64 v[20:21], v[28:29], 0, s[16:17]
	v_lshl_add_u64 v[24:25], v[28:29], 0, s[14:15]
	v_lshl_add_u64 v[30:31], v[28:29], 0, s[12:13]
	v_lshl_add_u64 v[32:33], v[28:29], 0, s[2:3]
	v_mov_b32_e32 v4, v176
	v_mov_b32_e32 v5, v177
	v_mov_b32_e32 v6, v178
	v_mov_b32_e32 v7, v179
	v_mov_b32_e32 v8, v206
	v_mov_b32_e32 v9, v207
	v_mov_b32_e32 v10, v208
	v_mov_b32_e32 v11, v209
	v_mov_b32_e32 v12, v210
	v_mov_b32_e32 v13, v211
	v_mov_b32_e32 v14, v212
	v_mov_b32_e32 v15, v213
	v_mov_b32_e32 v16, v214
	v_mov_b32_e32 v17, v215
	v_mov_b32_e32 v18, v216
	v_mov_b32_e32 v19, v217
	v_mov_b32_e32 v20, v222
	v_mov_b32_e32 v21, v223
	v_mov_b32_e32 v22, v224
	v_mov_b32_e32 v23, v225
	v_mov_b32_e32 v24, v226
	v_mov_b32_e32 v25, v227
	v_mov_b32_e32 v26, v228
	v_mov_b32_e32 v27, v229
	v_mov_b32_e32 v28, v230
	v_mov_b32_e32 v29, v231
	v_mov_b32_e32 v30, v232
	v_mov_b32_e32 v31, v233
	v_mov_b32_e32 v32, v234
	v_mov_b32_e32 v33, v235
	v_mov_b32_e32 v34, v236
	v_mov_b32_e32 v35, v237
	v_ashrrev_i32_e32 v39, 6, v38
	v_lshlrev_b32_e32 v37, 9, v38
	v_bitop3_b32 v39, v39, v38, 7 bitop3:0x78
	v_lshrrev_b32_e32 v2, 2, v38
	v_and_b32_e32 v37, 0x1e00, v37
	v_lshlrev_b32_e32 v39, 4, v39
	v_add3_u32 v39, 0, v37, v39
	v_and_b32_e32 v48, 12, v2
	v_ashrrev_i32_e32 v37, 3, v38
	v_lshrrev_b32_e32 v49, 5, v38
	v_add_u32_e32 v48, v39, v48
	v_and_b32_e32 v2, 0x70, v36
	v_add_u32_e32 v36, s46, v37
	s_mov_b64 s[2:3], -1
	s_and_b64 vcc, exec, s[0:1]
	v_lshlrev_b32_e32 v37, 7, v37
	v_xor_b32_e32 v82, v49, v38
	v_mul_f32_e32 v49, 0x42000000, v95
	v_mul_f32_e32 v50, 0x42000000, v63
	v_mul_f32_e32 v52, 0x42000000, v73
	v_mul_f32_e32 v54, 0x42000000, v69
	v_mul_f32_e32 v51, 0x42000000, v94
	v_mul_f32_e32 v53, 0x42000000, v62
	v_mul_f32_e32 v57, 0x42000000, v72
	v_mul_f32_e32 v58, 0x42000000, v68
	v_mul_f32_e32 v55, 0x42000000, v93
	v_mul_f32_e32 v56, 0x42000000, v61
	v_mul_f32_e32 v61, 0x42000000, v71
	v_mul_f32_e32 v62, 0x42000000, v67
	v_mul_f32_e32 v59, 0x42000000, v92
	v_mul_f32_e32 v60, 0x42000000, v60
	v_mul_f32_e32 v64, 0x42000000, v70
	v_mul_f32_e32 v65, 0x42000000, v66
	v_mul_f32_e32 v66, 0x42000000, v79
	v_mul_f32_e32 v67, 0x42000000, v47
	v_mul_f32_e32 v69, 0x42000000, v43
	v_mul_f32_e32 v71, 0x42000000, v87
	v_mul_f32_e32 v68, 0x42000000, v78
	v_mul_f32_e32 v70, 0x42000000, v46
	v_mul_f32_e32 v74, 0x42000000, v42
	v_mul_f32_e32 v75, 0x42000000, v86
	v_mul_f32_e32 v72, 0x42000000, v77
	v_mul_f32_e32 v73, 0x42000000, v45
	v_mul_f32_e32 v78, 0x42000000, v41
	v_mul_f32_e32 v79, 0x42000000, v85
	v_mul_f32_e32 v76, 0x42000000, v76
	v_mul_f32_e32 v77, 0x42000000, v44
	v_mul_f32_e32 v80, 0x42000000, v40
	v_mul_f32_e32 v81, 0x42000000, v84
	v_add_u32_e32 v63, 0x2000, v48
	v_add_u32_e32 v47, 0x4000, v48
	v_add_u32_e32 v46, 0x6000, v48
	s_barrier
	s_cbranch_vccz .LBB0_802
	v_mov_b32_e32 v118, v3
	v_mov_b32_e32 v119, v3
	v_cvt_pk_fp8_f32 v118, v81, v80
	v_cvt_pk_fp8_f32 v119, v79, v78
	v_mul_f32_e32 v116, 0x42000000, v8
	v_mul_f32_e32 v117, 0x42000000, v4
	v_cvt_pk_fp8_f32 v118, v77, v76 op_sel:[0,0,1]
	v_cvt_pk_fp8_f32 v119, v73, v72 op_sel:[0,0,1]
	v_mul_f32_e32 v114, 0x42000000, v16
	v_mul_f32_e32 v115, 0x42000000, v12
	v_mul_f32_e32 v112, 0x42000000, v9
	ds_write2_b32 v48, v118, v119 offset1:32
	v_mov_b32_e32 v118, v3
	v_mov_b32_e32 v119, v3
	v_cvt_pk_fp8_f32 v118, v75, v74
	v_cvt_pk_fp8_f32 v119, v71, v69
	v_mul_f32_e32 v113, 0x42000000, v5
	v_mul_f32_e32 v110, 0x42000000, v17
	v_cvt_pk_fp8_f32 v118, v70, v68 op_sel:[0,0,1]
	v_cvt_pk_fp8_f32 v119, v67, v66 op_sel:[0,0,1]
	v_mul_f32_e32 v111, 0x42000000, v13
	v_mul_f32_e32 v108, 0x42000000, v10
	v_mul_f32_e32 v109, 0x42000000, v6
	ds_write2_b32 v48, v118, v119 offset0:64 offset1:96
	v_mov_b32_e32 v118, v3
	v_mov_b32_e32 v119, v3
	v_cvt_pk_fp8_f32 v118, v65, v64
	v_cvt_pk_fp8_f32 v119, v62, v61
	v_mul_f32_e32 v106, 0x42000000, v18
	v_mul_f32_e32 v107, 0x42000000, v14
	v_cvt_pk_fp8_f32 v118, v60, v59 op_sel:[0,0,1]
	v_cvt_pk_fp8_f32 v119, v56, v55 op_sel:[0,0,1]
	v_mul_f32_e32 v104, 0x42000000, v11
	v_mul_f32_e32 v105, 0x42000000, v7
	v_mul_f32_e32 v102, 0x42000000, v19
	ds_write2_b32 v63, v118, v119 offset1:32
	v_mov_b32_e32 v118, v3
	v_mov_b32_e32 v119, v3
	v_cvt_pk_fp8_f32 v118, v58, v57
	v_cvt_pk_fp8_f32 v119, v54, v52
	v_mul_f32_e32 v103, 0x42000000, v15
	v_mul_f32_e32 v100, 0x42000000, v24
	v_cvt_pk_fp8_f32 v118, v53, v51 op_sel:[0,0,1]
	v_cvt_pk_fp8_f32 v119, v50, v49 op_sel:[0,0,1]
	v_mul_f32_e32 v101, 0x42000000, v20
	v_mul_f32_e32 v98, 0x42000000, v32
	v_mul_f32_e32 v99, 0x42000000, v28
	ds_write2_b32 v63, v118, v119 offset0:64 offset1:96
	v_mov_b32_e32 v118, v3
	v_cvt_pk_fp8_f32 v118, v117, v116
	v_mul_f32_e32 v96, 0x42000000, v25
	v_mul_f32_e32 v97, 0x42000000, v21
	v_mul_f32_e32 v94, 0x42000000, v33
	v_cvt_pk_fp8_f32 v118, v115, v114 op_sel:[0,0,1]
	v_mov_b32_e32 v114, v3
	v_cvt_pk_fp8_f32 v114, v113, v112
	v_mul_f32_e32 v95, 0x42000000, v29
	v_mul_f32_e32 v92, 0x42000000, v26
	v_mul_f32_e32 v93, 0x42000000, v22
	v_cvt_pk_fp8_f32 v114, v111, v110 op_sel:[0,0,1]
	v_mov_b32_e32 v110, v3
	v_cvt_pk_fp8_f32 v110, v109, v108
	s_lshl_b64 s[0:1], s[10:11], 20
	s_add_u32 s0, s41, s0
	v_lshlrev_b32_e32 v40, 4, v82
	v_cvt_pk_fp8_f32 v110, v107, v106 op_sel:[0,0,1]
	v_mov_b32_e32 v106, v3
	v_cvt_pk_fp8_f32 v106, v105, v104
	v_mul_f32_e32 v88, 0x42000000, v34
	v_mul_f32_e32 v89, 0x42000000, v30
	s_addc_u32 s1, s42, s1
	v_cvt_pk_fp8_f32 v106, v103, v102 op_sel:[0,0,1]
	v_mov_b32_e32 v102, v3
	v_cvt_pk_fp8_f32 v102, v101, v100
	v_and_b32_e32 v40, 0x70, v40
	v_mul_f32_e32 v86, 0x42000000, v27
	v_mul_f32_e32 v87, 0x42000000, v23
	v_cvt_pk_fp8_f32 v102, v99, v98 op_sel:[0,0,1]
	v_mov_b32_e32 v98, v3
	v_cvt_pk_fp8_f32 v98, v97, v96
	s_add_u32 s0, s0, s45
	v_add_u32_e32 v84, 0xfffff800, v36
	v_add_u32_e32 v38, 0xfffff8c0, v36
	v_cvt_pk_fp8_f32 v98, v95, v94 op_sel:[0,0,1]
	v_mov_b32_e32 v94, v3
	v_cvt_pk_fp8_f32 v94, v93, v92
	v_add3_u32 v83, 0, v37, v40
	v_add_u32_e32 v40, 0xfffff880, v36
	v_add_u32_e32 v42, 0xfffff840, v36
	v_cvt_pk_fp8_f32 v94, v89, v88 op_sel:[0,0,1]
	v_mov_b32_e32 v88, v3
	v_cvt_pk_fp8_f32 v88, v87, v86
	s_addc_u32 s1, s1, 0
	v_ashrrev_i32_e32 v39, 31, v38
	v_ashrrev_i32_e32 v41, 31, v40
	v_ashrrev_i32_e32 v43, 31, v42
	v_ashrrev_i32_e32 v85, 31, v84
	v_lshl_add_u64 v[44:45], s[0:1], 0, v[2:3]
	v_lshlrev_b64 v[38:39], 10, v[38:39]
	v_lshlrev_b64 v[40:41], 10, v[40:41]
	v_lshlrev_b64 v[42:43], 10, v[42:43]
	v_lshlrev_b64 v[84:85], 10, v[84:85]
	v_lshl_add_u64 v[38:39], v[44:45], 0, v[38:39]
	v_lshl_add_u64 v[40:41], v[44:45], 0, v[40:41]
	v_lshl_add_u64 v[42:43], v[44:45], 0, v[42:43]
	v_lshl_add_u64 v[44:45], v[44:45], 0, v[84:85]
	v_mul_f32_e32 v84, 0x42000000, v35
	v_mul_f32_e32 v85, 0x42000000, v31
	v_cvt_pk_fp8_f32 v88, v85, v84 op_sel:[0,0,1]
	ds_write2_b32 v47, v118, v114 offset1:32
	ds_write2_b32 v47, v110, v106 offset0:64 offset1:96
	ds_write2_b32 v46, v102, v98 offset1:32
	ds_write2_b32 v46, v94, v88 offset0:64 offset1:96
	s_waitcnt lgkmcnt(0)
	s_barrier
	ds_read_b128 v[84:87], v83
	s_mov_b64 s[2:3], 0
	s_waitcnt lgkmcnt(0)
	global_store_dwordx4 v[44:45], v[84:87], off
	ds_read_b128 v[84:87], v83 offset:8192
	s_waitcnt lgkmcnt(0)
	global_store_dwordx4 v[42:43], v[84:87], off
	ds_read_b128 v[42:45], v83 offset:16384
	s_waitcnt lgkmcnt(0)
	global_store_dwordx4 v[40:41], v[42:45], off
	ds_read_b128 v[40:43], v83 offset:24576
	s_waitcnt lgkmcnt(0)
	global_store_dwordx4 v[38:39], v[40:43], off
	s_barrier

.LBB0_1265:
	v_mov_b32_e32 v8, v0
	v_ashrrev_i32_e32 v181, 31, v180
	v_ashrrev_i32_e32 v2, 2, v8
	v_and_b32_e32 v6, 0xffffffc0, v2
	v_lshlrev_b64 v[4:5], 8, v[180:181]
	v_ashrrev_i32_e32 v7, 31, v6
	v_and_or_b32 v6, v8, 15, v6
	v_bfe_u32 v12, v8, 4, 1
	v_lshl_add_u64 v[10:11], v[6:7], 0, v[4:5]
	v_lshlrev_b32_e32 v4, 3, v12
	v_lshrrev_b32_e32 v2, 1, v8
	v_sub_co_u32_e32 v8, vcc, 0, v4
	v_min_f32_e32 v4, 0x40e00000, v176
	s_nop 0
	v_subb_co_u32_e64 v9, s[2:3], 0, 0, vcc
	s_mov_b32 s2, 0xc1c00000
	v_med3_f32 v5, v172, s2, v200
	v_mul_f32_e32 v5, v4, v5
	v_mul_f32_e32 v4, 0xc01d265f, v4
	v_exp_f32_e32 v4, v4
	v_med3_f32 v6, v173, s2, v200
	v_med3_f32 v7, v174, s2, v200
	v_med3_f32 v13, v175, s2, v200
	v_add_f32_e32 v4, 1.0, v4
	v_rcp_f32_e32 v4, v4
	v_med3_f32 v14, v164, s2, v200
	v_med3_f32 v15, v165, s2, v200
	v_med3_f32 v16, v166, s2, v200
	v_mul_f32_e32 v5, v4, v5
	v_min_f32_e32 v4, 0x40e00000, v177
	v_mul_f32_e32 v6, v4, v6
	v_mul_f32_e32 v4, 0xc01d265f, v4
	v_exp_f32_e32 v4, v4
	v_med3_f32 v17, v167, s2, v200
	v_med3_f32 v18, v150, s2, v200
	v_med3_f32 v19, v151, s2, v200
	v_add_f32_e32 v4, 1.0, v4
	v_rcp_f32_e32 v4, v4
	v_lshlrev_b32_e32 v12, 4, v12
	s_lshl_b32 s12, s26, 7
	s_ashr_i32 s13, s12, 31
	v_mul_f32_e32 v6, v4, v6
	v_min_f32_e32 v4, 0x40e00000, v178
	v_mul_f32_e32 v7, v4, v7
	v_mul_f32_e32 v4, 0xc01d265f, v4
	v_exp_f32_e32 v4, v4
	v_and_b32_e32 v2, 0x78, v2
	v_med3_f32 v20, v87, s2, v200
	s_and_b64 vcc, exec, s[40:41]
	v_add_f32_e32 v4, 1.0, v4
	v_rcp_f32_e32 v4, v4
	s_nop 0
	v_mul_f32_e32 v7, v4, v7
	v_min_f32_e32 v4, 0x40e00000, v179
	v_mul_f32_e32 v13, v4, v13
	v_mul_f32_e32 v4, 0xc01d265f, v4
	v_exp_f32_e32 v4, v4
	s_nop 0
	v_add_f32_e32 v4, 1.0, v4
	v_rcp_f32_e32 v4, v4
	s_nop 0
	v_mul_f32_e32 v13, v4, v13
	v_min_f32_e32 v4, 0x40e00000, v168
	v_mul_f32_e32 v14, v4, v14
	v_mul_f32_e32 v4, 0xc01d265f, v4
	v_exp_f32_e32 v4, v4
	s_nop 0
	v_add_f32_e32 v4, 1.0, v4
	v_rcp_f32_e32 v4, v4
	s_nop 0
	v_mul_f32_e32 v14, v4, v14
	v_min_f32_e32 v4, 0x40e00000, v169
	v_mul_f32_e32 v15, v4, v15
	v_mul_f32_e32 v4, 0xc01d265f, v4
	v_exp_f32_e32 v4, v4
	s_nop 0
	v_add_f32_e32 v4, 1.0, v4
	v_rcp_f32_e32 v4, v4
	s_nop 0
	v_mul_f32_e32 v15, v4, v15
	v_min_f32_e32 v4, 0x40e00000, v170
	v_mul_f32_e32 v16, v4, v16
	v_mul_f32_e32 v4, 0xc01d265f, v4
	v_exp_f32_e32 v4, v4
	s_nop 0
	v_add_f32_e32 v4, 1.0, v4
	v_rcp_f32_e32 v4, v4
	s_nop 0
	v_mul_f32_e32 v16, v4, v16
	v_min_f32_e32 v4, 0x40e00000, v171
	v_mul_f32_e32 v17, v4, v17
	v_mul_f32_e32 v4, 0xc01d265f, v4
	v_exp_f32_e32 v4, v4
	s_nop 0
	v_add_f32_e32 v4, 1.0, v4
	v_rcp_f32_e32 v4, v4
	s_nop 0
	v_mul_f32_e32 v17, v4, v17
	v_mov_b32_e32 v4, v3
	v_cvt_pk_fp8_f32 v4, v5, v6
	v_min_f32_e32 v6, 0x40e00000, v160
	v_mov_b32_e32 v5, v3
	v_cvt_pk_fp8_f32 v4, v7, v13 op_sel:[0,0,1]
	v_med3_f32 v7, v156, s2, v200
	v_mul_f32_e32 v7, v6, v7
	v_mul_f32_e32 v6, 0xc01d265f, v6
	v_exp_f32_e32 v6, v6
	v_med3_f32 v13, v157, s2, v200
	v_cvt_pk_fp8_f32 v5, v14, v15
	v_med3_f32 v14, v158, s2, v200
	v_add_f32_e32 v6, 1.0, v6
	v_rcp_f32_e32 v6, v6
	v_med3_f32 v15, v159, s2, v200
	v_cvt_pk_fp8_f32 v5, v16, v17 op_sel:[0,0,1]
	v_med3_f32 v16, v148, s2, v200
	v_mul_f32_e32 v7, v6, v7
	v_min_f32_e32 v6, 0x40e00000, v161
	v_mul_f32_e32 v13, v6, v13
	v_mul_f32_e32 v6, 0xc01d265f, v6
	v_exp_f32_e32 v6, v6
	v_med3_f32 v17, v149, s2, v200
	v_add_f32_e32 v6, 1.0, v6
	v_rcp_f32_e32 v6, v6
	s_nop 0
	v_mul_f32_e32 v13, v6, v13
	v_min_f32_e32 v6, 0x40e00000, v162
	v_mul_f32_e32 v14, v6, v14
	v_mul_f32_e32 v6, 0xc01d265f, v6
	v_exp_f32_e32 v6, v6
	s_nop 0
	v_add_f32_e32 v6, 1.0, v6
	v_rcp_f32_e32 v6, v6
	s_nop 0
	v_mul_f32_e32 v14, v6, v14
	v_min_f32_e32 v6, 0x40e00000, v163
	v_mul_f32_e32 v15, v6, v15
	v_mul_f32_e32 v6, 0xc01d265f, v6
	v_exp_f32_e32 v6, v6
	s_nop 0
	v_add_f32_e32 v6, 1.0, v6
	v_rcp_f32_e32 v6, v6
	s_nop 0
	v_mul_f32_e32 v15, v6, v15
	v_min_f32_e32 v6, 0x40e00000, v152
	v_mul_f32_e32 v16, v6, v16
	v_mul_f32_e32 v6, 0xc01d265f, v6
	v_exp_f32_e32 v6, v6
	s_nop 0
	v_add_f32_e32 v6, 1.0, v6
	v_rcp_f32_e32 v6, v6
	s_nop 0
	v_mul_f32_e32 v16, v6, v16
	v_min_f32_e32 v6, 0x40e00000, v153
	v_mul_f32_e32 v17, v6, v17
	v_mul_f32_e32 v6, 0xc01d265f, v6
	v_exp_f32_e32 v6, v6
	s_nop 0
	v_add_f32_e32 v6, 1.0, v6
	v_rcp_f32_e32 v6, v6
	s_nop 0
	v_mul_f32_e32 v17, v6, v17
	v_min_f32_e32 v6, 0x40e00000, v154
	v_mul_f32_e32 v18, v6, v18
	v_mul_f32_e32 v6, 0xc01d265f, v6
	v_exp_f32_e32 v6, v6
	s_nop 0
	v_add_f32_e32 v6, 1.0, v6
	v_rcp_f32_e32 v6, v6
	s_nop 0
	v_mul_f32_e32 v18, v6, v18
	v_min_f32_e32 v6, 0x40e00000, v155
	v_mul_f32_e32 v19, v6, v19
	v_mul_f32_e32 v6, 0xc01d265f, v6
	v_exp_f32_e32 v6, v6
	s_nop 0
	v_add_f32_e32 v6, 1.0, v6
	v_rcp_f32_e32 v6, v6
	s_nop 0
	v_mul_f32_e32 v19, v6, v19
	v_mov_b32_e32 v6, v3
	v_cvt_pk_fp8_f32 v6, v7, v13
	v_mov_b32_e32 v7, v3
	v_cvt_pk_fp8_f32 v7, v16, v17
	v_med3_f32 v13, v143, s2, v200
	v_cvt_pk_fp8_f32 v6, v14, v15 op_sel:[0,0,1]
	v_or_b32_e32 v14, v10, v12
	v_mov_b32_e32 v15, v11
	v_cvt_pk_fp8_f32 v7, v18, v19 op_sel:[0,0,1]
	v_lshlrev_b64 v[14:15], 10, v[14:15]
	v_lshl_add_u64 v[14:15], s[10:11], 0, v[14:15]
	v_lshl_add_u64 v[14:15], v[14:15], 0, s[12:13]
	v_lshl_add_u64 v[14:15], v[14:15], 0, v[2:3]
	v_permlane16_swap_b32_e32 v4, v6
	v_permlane16_swap_b32_e32 v5, v7
	v_lshl_add_u64 v[14:15], v[14:15], 0, v[8:9]
	global_store_dwordx4 v[14:15], v[4:7], off
	v_med3_f32 v14, v132, s2, v200
	v_med3_f32 v15, v133, s2, v200
	v_min_f32_e32 v4, 0x40e00000, v144
	v_med3_f32 v5, v140, s2, v200
	v_mul_f32_e32 v5, v4, v5
	v_mul_f32_e32 v4, 0xc01d265f, v4
	v_exp_f32_e32 v4, v4
	v_med3_f32 v6, v141, s2, v200
	v_med3_f32 v7, v142, s2, v200
	v_med3_f32 v16, v134, s2, v200
	v_add_f32_e32 v4, 1.0, v4
	v_rcp_f32_e32 v4, v4
	v_med3_f32 v17, v135, s2, v200
	v_med3_f32 v18, v118, s2, v200
	v_med3_f32 v19, v119, s2, v200
	v_mul_f32_e32 v5, v4, v5
	v_min_f32_e32 v4, 0x40e00000, v145
	v_mul_f32_e32 v6, v4, v6
	v_mul_f32_e32 v4, 0xc01d265f, v4
	v_exp_f32_e32 v4, v4
	s_nop 0
	v_add_f32_e32 v4, 1.0, v4
	v_rcp_f32_e32 v4, v4
	s_nop 0
	v_mul_f32_e32 v6, v4, v6
	v_min_f32_e32 v4, 0x40e00000, v146
	v_mul_f32_e32 v7, v4, v7
	v_mul_f32_e32 v4, 0xc01d265f, v4
	v_exp_f32_e32 v4, v4
	s_nop 0
	v_add_f32_e32 v4, 1.0, v4
	v_rcp_f32_e32 v4, v4
	s_nop 0
	v_mul_f32_e32 v7, v4, v7
	v_min_f32_e32 v4, 0x40e00000, v147
	v_mul_f32_e32 v13, v4, v13
	v_mul_f32_e32 v4, 0xc01d265f, v4
	v_exp_f32_e32 v4, v4
	s_nop 0
	v_add_f32_e32 v4, 1.0, v4
	v_rcp_f32_e32 v4, v4
	s_nop 0
	v_mul_f32_e32 v13, v4, v13
	v_min_f32_e32 v4, 0x40e00000, v136
	v_mul_f32_e32 v14, v4, v14
	v_mul_f32_e32 v4, 0xc01d265f, v4
	v_exp_f32_e32 v4, v4
	s_nop 0
	v_add_f32_e32 v4, 1.0, v4
	v_rcp_f32_e32 v4, v4
	s_nop 0
	v_mul_f32_e32 v14, v4, v14
	v_min_f32_e32 v4, 0x40e00000, v137
	v_mul_f32_e32 v15, v4, v15
	v_mul_f32_e32 v4, 0xc01d265f, v4
	v_exp_f32_e32 v4, v4
	s_nop 0
	v_add_f32_e32 v4, 1.0, v4
	v_rcp_f32_e32 v4, v4
	s_nop 0
	v_mul_f32_e32 v15, v4, v15
	v_min_f32_e32 v4, 0x40e00000, v138
	v_mul_f32_e32 v16, v4, v16
	v_mul_f32_e32 v4, 0xc01d265f, v4
	v_exp_f32_e32 v4, v4
	s_nop 0
	v_add_f32_e32 v4, 1.0, v4
	v_rcp_f32_e32 v4, v4
	s_nop 0
	v_mul_f32_e32 v16, v4, v16
	v_min_f32_e32 v4, 0x40e00000, v139
	v_mul_f32_e32 v17, v4, v17
	v_mul_f32_e32 v4, 0xc01d265f, v4
	v_exp_f32_e32 v4, v4
	s_nop 0
	v_add_f32_e32 v4, 1.0, v4
	v_rcp_f32_e32 v4, v4
	s_nop 0
	v_mul_f32_e32 v17, v4, v17
	v_mov_b32_e32 v4, v3
	v_cvt_pk_fp8_f32 v4, v5, v6
	v_min_f32_e32 v6, 0x40e00000, v128
	v_mov_b32_e32 v5, v3
	v_cvt_pk_fp8_f32 v4, v7, v13 op_sel:[0,0,1]
	v_med3_f32 v7, v124, s2, v200
	v_mul_f32_e32 v7, v6, v7
	v_mul_f32_e32 v6, 0xc01d265f, v6
	v_exp_f32_e32 v6, v6
	v_med3_f32 v13, v125, s2, v200
	v_cvt_pk_fp8_f32 v5, v14, v15
	v_med3_f32 v14, v126, s2, v200
	v_add_f32_e32 v6, 1.0, v6
	v_rcp_f32_e32 v6, v6
	v_med3_f32 v15, v127, s2, v200
	v_cvt_pk_fp8_f32 v5, v16, v17 op_sel:[0,0,1]
	v_med3_f32 v16, v116, s2, v200
	v_mul_f32_e32 v7, v6, v7
	v_min_f32_e32 v6, 0x40e00000, v129
	v_mul_f32_e32 v13, v6, v13
	v_mul_f32_e32 v6, 0xc01d265f, v6
	v_exp_f32_e32 v6, v6
	v_med3_f32 v17, v117, s2, v200
	v_add_f32_e32 v6, 1.0, v6
	v_rcp_f32_e32 v6, v6
	s_nop 0
	v_mul_f32_e32 v13, v6, v13
	v_min_f32_e32 v6, 0x40e00000, v130
	v_mul_f32_e32 v14, v6, v14
	v_mul_f32_e32 v6, 0xc01d265f, v6
	v_exp_f32_e32 v6, v6
	s_nop 0
	v_add_f32_e32 v6, 1.0, v6
	v_rcp_f32_e32 v6, v6
	s_nop 0
	v_mul_f32_e32 v14, v6, v14
	v_min_f32_e32 v6, 0x40e00000, v131
	v_mul_f32_e32 v15, v6, v15
	v_mul_f32_e32 v6, 0xc01d265f, v6
	v_exp_f32_e32 v6, v6
	s_nop 0
	v_add_f32_e32 v6, 1.0, v6
	v_rcp_f32_e32 v6, v6
	s_nop 0
	v_mul_f32_e32 v15, v6, v15
	v_min_f32_e32 v6, 0x40e00000, v120
	v_mul_f32_e32 v16, v6, v16
	v_mul_f32_e32 v6, 0xc01d265f, v6
	v_exp_f32_e32 v6, v6
	s_nop 0
	v_add_f32_e32 v6, 1.0, v6
	v_rcp_f32_e32 v6, v6
	s_nop 0
	v_mul_f32_e32 v16, v6, v16
	v_min_f32_e32 v6, 0x40e00000, v121
	v_mul_f32_e32 v17, v6, v17
	v_mul_f32_e32 v6, 0xc01d265f, v6
	v_exp_f32_e32 v6, v6
	s_nop 0
	v_add_f32_e32 v6, 1.0, v6
	v_rcp_f32_e32 v6, v6
	s_nop 0
	v_mul_f32_e32 v17, v6, v17
	v_min_f32_e32 v6, 0x40e00000, v122
	v_mul_f32_e32 v18, v6, v18
	v_mul_f32_e32 v6, 0xc01d265f, v6
	v_exp_f32_e32 v6, v6
	s_nop 0
	v_add_f32_e32 v6, 1.0, v6
	v_rcp_f32_e32 v6, v6
	s_nop 0
	v_mul_f32_e32 v18, v6, v18
	v_min_f32_e32 v6, 0x40e00000, v123
	v_mul_f32_e32 v19, v6, v19
	v_mul_f32_e32 v6, 0xc01d265f, v6
	v_exp_f32_e32 v6, v6
	s_nop 0
	v_add_f32_e32 v6, 1.0, v6
	v_rcp_f32_e32 v6, v6
	s_nop 0
	v_mul_f32_e32 v19, v6, v19
	v_mov_b32_e32 v6, v3
	v_cvt_pk_fp8_f32 v6, v7, v13
	v_mov_b32_e32 v7, v3
	v_cvt_pk_fp8_f32 v7, v16, v17
	v_or_b32_e32 v13, 32, v12
	v_cvt_pk_fp8_f32 v6, v14, v15 op_sel:[0,0,1]
	v_or_b32_e32 v14, v10, v13
	v_mov_b32_e32 v15, v11
	v_cvt_pk_fp8_f32 v7, v18, v19 op_sel:[0,0,1]
	v_lshlrev_b64 v[14:15], 10, v[14:15]
	v_lshl_add_u64 v[14:15], s[10:11], 0, v[14:15]
	v_lshl_add_u64 v[14:15], v[14:15], 0, s[12:13]
	v_lshl_add_u64 v[14:15], v[14:15], 0, v[2:3]
	v_permlane16_swap_b32_e32 v4, v6
	v_permlane16_swap_b32_e32 v5, v7
	v_lshl_add_u64 v[14:15], v[14:15], 0, v[8:9]
	global_store_dwordx4 v[14:15], v[4:7], off
	v_med3_f32 v14, v111, s2, v200
	v_med3_f32 v15, v100, s2, v200
	v_min_f32_e32 v4, 0x40e00000, v112
	v_med3_f32 v5, v108, s2, v200
	v_mul_f32_e32 v5, v4, v5
	v_mul_f32_e32 v4, 0xc01d265f, v4
	v_exp_f32_e32 v4, v4
	v_med3_f32 v6, v109, s2, v200
	v_med3_f32 v7, v110, s2, v200
	v_med3_f32 v16, v101, s2, v200
	v_add_f32_e32 v4, 1.0, v4
	v_rcp_f32_e32 v4, v4
	v_med3_f32 v17, v102, s2, v200
	v_med3_f32 v18, v103, s2, v200
	v_med3_f32 v19, v86, s2, v200
	v_mul_f32_e32 v5, v4, v5
	v_min_f32_e32 v4, 0x40e00000, v113
	v_mul_f32_e32 v6, v4, v6
	v_mul_f32_e32 v4, 0xc01d265f, v4
	v_exp_f32_e32 v4, v4
	v_lshl_add_u64 v[10:11], v[10:11], 0, s[52:53]
	v_add_f32_e32 v4, 1.0, v4
	v_rcp_f32_e32 v4, v4
	s_nop 0
	v_mul_f32_e32 v6, v4, v6
	v_min_f32_e32 v4, 0x40e00000, v114
	v_mul_f32_e32 v7, v4, v7
	v_mul_f32_e32 v4, 0xc01d265f, v4
	v_exp_f32_e32 v4, v4
	s_nop 0
	v_add_f32_e32 v4, 1.0, v4
	v_rcp_f32_e32 v4, v4
	s_nop 0
	v_mul_f32_e32 v7, v4, v7
	v_min_f32_e32 v4, 0x40e00000, v115
	v_mul_f32_e32 v14, v4, v14
	v_mul_f32_e32 v4, 0xc01d265f, v4
	v_exp_f32_e32 v4, v4
	s_nop 0
	v_add_f32_e32 v4, 1.0, v4
	v_rcp_f32_e32 v4, v4
	s_nop 0
	v_mul_f32_e32 v14, v4, v14
	v_min_f32_e32 v4, 0x40e00000, v104
	v_mul_f32_e32 v15, v4, v15
	v_mul_f32_e32 v4, 0xc01d265f, v4
	v_exp_f32_e32 v4, v4
	s_nop 0
	v_add_f32_e32 v4, 1.0, v4
	v_rcp_f32_e32 v4, v4
	s_nop 0
	v_mul_f32_e32 v15, v4, v15
	v_min_f32_e32 v4, 0x40e00000, v105
	v_mul_f32_e32 v16, v4, v16
	v_mul_f32_e32 v4, 0xc01d265f, v4
	v_exp_f32_e32 v4, v4
	s_nop 0
	v_add_f32_e32 v4, 1.0, v4
	v_rcp_f32_e32 v4, v4
	s_nop 0
	v_mul_f32_e32 v16, v4, v16
	v_min_f32_e32 v4, 0x40e00000, v106
	v_mul_f32_e32 v17, v4, v17
	v_mul_f32_e32 v4, 0xc01d265f, v4
	v_exp_f32_e32 v4, v4
	s_nop 0
	v_add_f32_e32 v4, 1.0, v4
	v_rcp_f32_e32 v4, v4
	s_nop 0
	v_mul_f32_e32 v17, v4, v17
	v_min_f32_e32 v4, 0x40e00000, v107
	v_mul_f32_e32 v18, v4, v18
	v_mul_f32_e32 v4, 0xc01d265f, v4
	v_exp_f32_e32 v4, v4
	s_nop 0
	v_add_f32_e32 v4, 1.0, v4
	v_rcp_f32_e32 v4, v4
	s_nop 0
	v_mul_f32_e32 v18, v4, v18
	v_mov_b32_e32 v4, v3
	v_cvt_pk_fp8_f32 v4, v5, v6
	v_min_f32_e32 v6, 0x40e00000, v96
	v_mov_b32_e32 v5, v3
	v_cvt_pk_fp8_f32 v4, v7, v14 op_sel:[0,0,1]
	v_med3_f32 v7, v92, s2, v200
	v_mul_f32_e32 v7, v6, v7
	v_mul_f32_e32 v6, 0xc01d265f, v6
	v_exp_f32_e32 v6, v6
	v_med3_f32 v14, v93, s2, v200
	v_cvt_pk_fp8_f32 v5, v15, v16
	v_med3_f32 v15, v94, s2, v200
	v_add_f32_e32 v6, 1.0, v6
	v_rcp_f32_e32 v6, v6
	v_med3_f32 v16, v95, s2, v200
	v_cvt_pk_fp8_f32 v5, v17, v18 op_sel:[0,0,1]
	v_med3_f32 v17, v84, s2, v200
	v_mul_f32_e32 v7, v6, v7
	v_min_f32_e32 v6, 0x40e00000, v97
	v_mul_f32_e32 v14, v6, v14
	v_mul_f32_e32 v6, 0xc01d265f, v6
	v_exp_f32_e32 v6, v6
	v_med3_f32 v18, v85, s2, v200
	v_add_f32_e32 v6, 1.0, v6
	v_rcp_f32_e32 v6, v6
	s_nop 0
	v_mul_f32_e32 v14, v6, v14
	v_min_f32_e32 v6, 0x40e00000, v98
	v_mul_f32_e32 v15, v6, v15
	v_mul_f32_e32 v6, 0xc01d265f, v6
	v_exp_f32_e32 v6, v6
	s_nop 0
	v_add_f32_e32 v6, 1.0, v6
	v_rcp_f32_e32 v6, v6
	s_nop 0
	v_mul_f32_e32 v15, v6, v15
	v_min_f32_e32 v6, 0x40e00000, v99
	v_mul_f32_e32 v16, v6, v16
	v_mul_f32_e32 v6, 0xc01d265f, v6
	v_exp_f32_e32 v6, v6
	s_nop 0
	v_add_f32_e32 v6, 1.0, v6
	v_rcp_f32_e32 v6, v6
	s_nop 0
	v_mul_f32_e32 v16, v6, v16
	v_min_f32_e32 v6, 0x40e00000, v88
	v_mul_f32_e32 v17, v6, v17
	v_mul_f32_e32 v6, 0xc01d265f, v6
	v_exp_f32_e32 v6, v6
	s_nop 0
	v_add_f32_e32 v6, 1.0, v6
	v_rcp_f32_e32 v6, v6
	s_nop 0
	v_mul_f32_e32 v17, v6, v17
	v_min_f32_e32 v6, 0x40e00000, v89
	v_mul_f32_e32 v18, v6, v18
	v_mul_f32_e32 v6, 0xc01d265f, v6
	v_exp_f32_e32 v6, v6
	s_nop 0
	v_add_f32_e32 v6, 1.0, v6
	v_rcp_f32_e32 v6, v6
	s_nop 0
	v_mul_f32_e32 v18, v6, v18
	v_min_f32_e32 v6, 0x40e00000, v90
	v_mul_f32_e32 v19, v6, v19
	v_mul_f32_e32 v6, 0xc01d265f, v6
	v_exp_f32_e32 v6, v6
	s_nop 0
	v_add_f32_e32 v6, 1.0, v6
	v_rcp_f32_e32 v6, v6
	s_nop 0
	v_mul_f32_e32 v19, v6, v19
	v_min_f32_e32 v6, 0x40e00000, v91
	v_mul_f32_e32 v20, v6, v20
	v_mul_f32_e32 v6, 0xc01d265f, v6
	v_exp_f32_e32 v6, v6
	s_nop 0
	v_add_f32_e32 v6, 1.0, v6
	v_rcp_f32_e32 v6, v6
	s_nop 0
	v_mul_f32_e32 v20, v6, v20
	v_mov_b32_e32 v6, v3
	v_cvt_pk_fp8_f32 v6, v7, v14
	v_mov_b32_e32 v7, v3
	v_cvt_pk_fp8_f32 v7, v17, v18
	v_or_b32_e32 v14, v10, v12
	v_cvt_pk_fp8_f32 v6, v15, v16 op_sel:[0,0,1]
	v_mov_b32_e32 v15, v11
	v_cvt_pk_fp8_f32 v7, v19, v20 op_sel:[0,0,1]
	v_lshlrev_b64 v[14:15], 10, v[14:15]
	v_lshl_add_u64 v[14:15], s[10:11], 0, v[14:15]
	v_lshl_add_u64 v[14:15], v[14:15], 0, s[12:13]
	v_lshl_add_u64 v[14:15], v[14:15], 0, v[2:3]
	v_permlane16_swap_b32_e32 v4, v6
	v_permlane16_swap_b32_e32 v5, v7
	v_lshl_add_u64 v[14:15], v[14:15], 0, v[8:9]
	global_store_dwordx4 v[14:15], v[4:7], off
	v_med3_f32 v12, v79, s2, v200
	v_med3_f32 v14, v68, s2, v200
	v_min_f32_e32 v4, 0x40e00000, v80
	v_med3_f32 v5, v76, s2, v200
	v_mul_f32_e32 v5, v4, v5
	v_mul_f32_e32 v4, 0xc01d265f, v4
	v_exp_f32_e32 v4, v4
	v_med3_f32 v6, v77, s2, v200
	v_med3_f32 v7, v78, s2, v200
	v_med3_f32 v15, v69, s2, v200
	v_add_f32_e32 v4, 1.0, v4
	v_rcp_f32_e32 v4, v4
	v_med3_f32 v16, v70, s2, v200
	v_med3_f32 v17, v71, s2, v200
	v_med3_f32 v18, v54, s2, v200
	v_mul_f32_e32 v5, v4, v5
	v_min_f32_e32 v4, 0x40e00000, v81
	v_mul_f32_e32 v6, v4, v6
	v_mul_f32_e32 v4, 0xc01d265f, v4
	v_exp_f32_e32 v4, v4
	v_med3_f32 v19, v55, s2, v200
	v_or_b32_e32 v10, v10, v13
	v_lshlrev_b64 v[10:11], 10, v[10:11]
	v_add_f32_e32 v4, 1.0, v4
	v_rcp_f32_e32 v4, v4
	v_lshl_add_u64 v[10:11], s[10:11], 0, v[10:11]
	v_lshl_add_u64 v[10:11], v[10:11], 0, s[12:13]
	v_lshl_add_u64 v[10:11], v[10:11], 0, v[2:3]
	v_mul_f32_e32 v6, v4, v6
	v_min_f32_e32 v4, 0x40e00000, v82
	v_mul_f32_e32 v7, v4, v7
	v_mul_f32_e32 v4, 0xc01d265f, v4
	v_exp_f32_e32 v4, v4
	v_lshl_add_u64 v[8:9], v[10:11], 0, v[8:9]
	v_add_f32_e32 v4, 1.0, v4
	v_rcp_f32_e32 v4, v4
	s_nop 0
	v_mul_f32_e32 v7, v4, v7
	v_min_f32_e32 v4, 0x40e00000, v83
	v_mul_f32_e32 v12, v4, v12
	v_mul_f32_e32 v4, 0xc01d265f, v4
	v_exp_f32_e32 v4, v4
	s_nop 0
	v_add_f32_e32 v4, 1.0, v4
	v_rcp_f32_e32 v4, v4
	s_nop 0
	v_mul_f32_e32 v12, v4, v12
	v_min_f32_e32 v4, 0x40e00000, v72
	v_mul_f32_e32 v14, v4, v14
	v_mul_f32_e32 v4, 0xc01d265f, v4
	v_exp_f32_e32 v4, v4
	s_nop 0
	v_add_f32_e32 v4, 1.0, v4
	v_rcp_f32_e32 v4, v4
	s_nop 0
	v_mul_f32_e32 v14, v4, v14
	v_min_f32_e32 v4, 0x40e00000, v73
	v_mul_f32_e32 v15, v4, v15
	v_mul_f32_e32 v4, 0xc01d265f, v4
	v_exp_f32_e32 v4, v4
	s_nop 0
	v_add_f32_e32 v4, 1.0, v4
	v_rcp_f32_e32 v4, v4
	s_nop 0
	v_mul_f32_e32 v15, v4, v15
	v_min_f32_e32 v4, 0x40e00000, v74
	v_mul_f32_e32 v16, v4, v16
	v_mul_f32_e32 v4, 0xc01d265f, v4
	v_exp_f32_e32 v4, v4
	s_nop 0
	v_add_f32_e32 v4, 1.0, v4
	v_rcp_f32_e32 v4, v4
	s_nop 0
	v_mul_f32_e32 v16, v4, v16
	v_min_f32_e32 v4, 0x40e00000, v75
	v_mul_f32_e32 v17, v4, v17
	v_mul_f32_e32 v4, 0xc01d265f, v4
	v_exp_f32_e32 v4, v4
	s_nop 0
	v_add_f32_e32 v4, 1.0, v4
	v_rcp_f32_e32 v4, v4
	s_nop 0
	v_mul_f32_e32 v17, v4, v17
	v_mov_b32_e32 v4, v3
	v_cvt_pk_fp8_f32 v4, v5, v6
	v_min_f32_e32 v6, 0x40e00000, v64
	v_mov_b32_e32 v5, v3
	v_cvt_pk_fp8_f32 v4, v7, v12 op_sel:[0,0,1]
	v_med3_f32 v7, v60, s2, v200
	v_mul_f32_e32 v7, v6, v7
	v_mul_f32_e32 v6, 0xc01d265f, v6
	v_exp_f32_e32 v6, v6
	v_med3_f32 v12, v61, s2, v200
	v_cvt_pk_fp8_f32 v5, v14, v15
	v_med3_f32 v14, v62, s2, v200
	v_add_f32_e32 v6, 1.0, v6
	v_rcp_f32_e32 v6, v6
	v_med3_f32 v15, v63, s2, v200
	v_cvt_pk_fp8_f32 v5, v16, v17 op_sel:[0,0,1]
	v_med3_f32 v16, v52, s2, v200
	v_mul_f32_e32 v7, v6, v7
	v_min_f32_e32 v6, 0x40e00000, v65
	v_mul_f32_e32 v12, v6, v12
	v_mul_f32_e32 v6, 0xc01d265f, v6
	v_exp_f32_e32 v6, v6
	v_med3_f32 v17, v53, s2, v200
	s_mov_b64 s[2:3], -1
	v_add_f32_e32 v6, 1.0, v6
	v_rcp_f32_e32 v6, v6
	s_nop 0
	v_mul_f32_e32 v12, v6, v12
	v_min_f32_e32 v6, 0x40e00000, v66
	v_mul_f32_e32 v14, v6, v14
	v_mul_f32_e32 v6, 0xc01d265f, v6
	v_exp_f32_e32 v6, v6
	s_nop 0
	v_add_f32_e32 v6, 1.0, v6
	v_rcp_f32_e32 v6, v6
	s_nop 0
	v_mul_f32_e32 v14, v6, v14
	v_min_f32_e32 v6, 0x40e00000, v67
	v_mul_f32_e32 v15, v6, v15
	v_mul_f32_e32 v6, 0xc01d265f, v6
	v_exp_f32_e32 v6, v6
	s_nop 0
	v_add_f32_e32 v6, 1.0, v6
	v_rcp_f32_e32 v6, v6
	s_nop 0
	v_mul_f32_e32 v15, v6, v15
	v_min_f32_e32 v6, 0x40e00000, v56
	v_mul_f32_e32 v16, v6, v16
	v_mul_f32_e32 v6, 0xc01d265f, v6
	v_exp_f32_e32 v6, v6
	s_nop 0
	v_add_f32_e32 v6, 1.0, v6
	v_rcp_f32_e32 v6, v6
	s_nop 0
	v_mul_f32_e32 v16, v6, v16
	v_min_f32_e32 v6, 0x40e00000, v57
	v_mul_f32_e32 v17, v6, v17
	v_mul_f32_e32 v6, 0xc01d265f, v6
	v_exp_f32_e32 v6, v6
	s_nop 0
	v_add_f32_e32 v6, 1.0, v6
	v_rcp_f32_e32 v6, v6
	s_nop 0
	v_mul_f32_e32 v17, v6, v17
	v_min_f32_e32 v6, 0x40e00000, v58
	v_mul_f32_e32 v18, v6, v18
	v_mul_f32_e32 v6, 0xc01d265f, v6
	v_exp_f32_e32 v6, v6
	s_nop 0
	v_add_f32_e32 v6, 1.0, v6
	v_rcp_f32_e32 v6, v6
	s_nop 0
	v_mul_f32_e32 v18, v6, v18
	v_min_f32_e32 v6, 0x40e00000, v59
	v_mul_f32_e32 v19, v6, v19
	v_mul_f32_e32 v6, 0xc01d265f, v6
	v_exp_f32_e32 v6, v6
	s_nop 0
	v_add_f32_e32 v6, 1.0, v6
	v_rcp_f32_e32 v6, v6
	s_nop 0
	v_mul_f32_e32 v19, v6, v19
	v_mov_b32_e32 v6, v3
	v_cvt_pk_fp8_f32 v6, v7, v12
	v_mov_b32_e32 v7, v3
	v_cvt_pk_fp8_f32 v7, v16, v17
	v_cvt_pk_fp8_f32 v6, v14, v15 op_sel:[0,0,1]
	v_cvt_pk_fp8_f32 v7, v18, v19 op_sel:[0,0,1]
	s_nop 0
	v_permlane16_swap_b32_e32 v4, v6
	v_permlane16_swap_b32_e32 v5, v7
	global_store_dwordx4 v[8:9], v[4:7], off
	s_cbranch_vccnz .LBB0_1269
	s_and_saveexec_b64 s[2:3], s[36:37]
	s_xor_b64 s[2:3], exec, s[2:3]
	s_cbranch_execz .LBB0_1268
	s_barrier
